# v55 + P10 emission pass prefetches stored scores two tiles ahead (parity-alternating buffers)
# baseline (speedup 1.0000x reference)
.LBB0_1226:
	v_add_u32_e32 v5, v4, v0
	v_ashrrev_i32_e32 v6, 1, v5
	v_bfe_u32 v5, v5, 16, 1
	v_add_u32_e32 v5, -1, v5
	s_movk_i32 s1, 0x7fff
	v_bitop3_b32 v5, v5, v6, s1 bitop3:0x78
	v_fma_f16 v5, v5, v2, v1
	v_max_f16_e32 v5, 0x6400, v5
	v_min_f16_e32 v5, 0x65ff, v5
	v_and_b32_e32 v5, 0x3ff, v5
	v_cmp_lt_i32_sdwa vcc, v3, v5 src0_sel:DWORD src1_sel:WORD_0
	s_add_i32 s0, s0, -1
	s_cmp_eq_u32 s0, 0
	v_cndmask_b32_e32 v0, v0, v6, vcc
	v_cndmask_b32_e32 v4, v6, v4, vcc
	s_cbranch_scc0 .LBB0_1226
	global_load_dwordx2 v[16:17], v[142:143], off sc1
	global_load_dwordx2 v[14:15], v[142:143], off offset:256 sc1
	s_bitcmp1_b32 s75, 0
	s_cbranch_scc0 .Lem_preY
	global_load_dwordx2 v[10:11], v[144:145], off sc1
	global_load_dwordx2 v[8:9], v[144:145], off offset:256 sc1
	s_branch .Lem_predone
.Lem_preY:
	global_load_dwordx2 v[188:189], v[144:145], off sc1
	global_load_dwordx2 v[190:191], v[144:145], off offset:256 sc1
.Lem_predone:
	v_and_b32_e32 v1, 0x8000, v0
	s_mov_b32 s0, 0xffff
	v_and_b32_e32 v2, 0xffff7fff, v0
	v_bitop3_b32 v0, v0, s0, v185 bitop3:0x6c
	v_cmp_eq_u32_e32 vcc, 0, v1
	v_mov_b32_e32 v52, v53
	v_mov_b32_e32 v54, v53
	v_cndmask_b32_e32 v0, v2, v0, vcc
	v_mov_b32_e32 v55, v53
	v_readlane_b32 s43, v0, 0
	v_readlane_b32 s86, v0, 1
	v_readlane_b32 s47, v0, 2
	v_readlane_b32 s46, v0, 3
	v_readlane_b32 s39, v0, 4
	v_readlane_b32 s38, v0, 5
	v_readlane_b32 s37, v0, 6
	v_readlane_b32 s36, v0, 7
	v_readlane_b32 s35, v0, 8
	v_readlane_b32 s34, v0, 9
	v_readlane_b32 s31, v0, 10
	v_readlane_b32 s30, v0, 11
	v_readlane_b32 s79, v0, 12
	v_readlane_b32 s78, v0, 13
	v_readlane_b32 s29, v0, 14
	v_readlane_b32 s28, v0, 15
	v_mov_b32_e32 v56, v53
	v_mov_b32_e32 v57, v53
	v_mov_b32_e32 v58, v53
	v_mov_b32_e32 v59, v53
	v_mov_b64_e32 v[0:1], v[52:53]
	s_mov_b32 s76, 0
	v_lshl_add_u64 v[12:13], v[144:145], 0, s[92:93]
	v_mov_b32_e32 v18, v138
	v_mov_b32_e32 v19, v180
	v_mov_b64_e32 v[2:3], v[54:55]
	v_mov_b64_e32 v[4:5], v[56:57]
	v_mov_b64_e32 v[6:7], v[58:59]
	s_mov_b32 s73, 0
	s_mov_b32 s84, 0
	s_mov_b32 s85, 0
	s_mov_b32 s24, 0
	s_mov_b32 s25, 0
	s_mov_b32 s26, 0
	s_mov_b32 s27, 0
	s_waitcnt vmcnt(2)
.LBB0_1228:
	s_cmp_lt_u32 s75, 2
	s_cbranch_scc1 .Lem_noissue
	s_bitcmp1_b32 s75, 0
	s_cbranch_scc1 .Lem_issueY
	global_load_dwordx2 v[10:11], v[12:13], off sc1
	global_load_dwordx2 v[8:9], v[12:13], off offset:256 sc1
	s_branch .Lem_noissue
.Lem_issueY:
	global_load_dwordx2 v[188:189], v[12:13], off sc1
	global_load_dwordx2 v[190:191], v[12:13], off offset:256 sc1
.Lem_noissue:
	v_cmp_le_f16_e32 vcc, s43, v16
	v_cmp_le_f16_e64 s[50:51], s86, v16
	s_and_saveexec_b64 s[54:55], vcc
	s_cbranch_execz .LBB0_1231
	v_mov_b32_e32 v20, s76
	v_mbcnt_lo_u32_b32 v20, vcc_lo, v20
	v_mbcnt_hi_u32_b32 v20, vcc_hi, v20
	v_cmp_gt_i32_e64 s[52:53], s48, v20
	s_and_b64 exec, exec, s[52:53]
	v_lshl_add_u32 v20, v20, 1, s33
	ds_write_b16 v20, v18 offset:24576

.LBB0_1263:
	v_cmp_le_f16_e64 s[54:55], s35, v14
	v_cmp_le_f16_e64 s[56:57], s34, v14
	s_and_saveexec_b64 s[0:1], s[54:55]
	s_cbranch_execz .LBB0_1266
	v_mov_b32_e32 v16, s24
	v_mbcnt_lo_u32_b32 v16, s54, v16
	v_mbcnt_hi_u32_b32 v16, s55, v16
	v_cmp_gt_i32_e64 s[58:59], s48, v16
	s_and_b64 exec, exec, s[58:59]
	v_lshl_add_u32 v16, v16, 1, s17
	ds_write_b16 v16, v18 offset:24576

.LBB0_1299:
	s_bcnt1_i32_b64 s0, vcc
	s_add_i32 s76, s76, s0
	s_bcnt1_i32_b64 s0, s[64:65]
	s_add_i32 s73, s73, s0
	s_bcnt1_i32_b64 s0, s[50:51]
	s_add_i32 s84, s84, s0
	s_bcnt1_i32_b64 s0, s[52:53]
	s_add_i32 s85, s85, s0
	s_bcnt1_i32_b64 s0, s[54:55]
	s_add_i32 s24, s24, s0
	s_bcnt1_i32_b64 s0, s[66:67]
	s_add_i32 s25, s25, s0
	s_bcnt1_i32_b64 s0, s[56:57]
	s_add_i32 s26, s26, s0
	s_bcnt1_i32_b64 s0, s[58:59]
	s_add_i32 s27, s27, s0
	s_add_i32 s75, s75, -1
	v_subrev_u32_e32 v19, 64, v19
	v_add_u32_e32 v18, 64, v18
	s_cmp_eq_u32 s75, 0
	v_lshl_add_u64 v[12:13], v[12:13], 0, s[92:93]
	s_cbranch_scc1 .LBB0_1301
	s_bitcmp1_b32 s75, 0
	s_cbranch_scc1 .Lem_copyY
	s_waitcnt vmcnt(3)
	v_mov_b64_e32 v[16:17], v[10:11]
	s_waitcnt vmcnt(2)
	v_mov_b64_e32 v[14:15], v[8:9]
	s_branch .LBB0_1228
.Lem_copyY:
	s_waitcnt vmcnt(3)
	v_mov_b64_e32 v[16:17], v[188:189]
	s_waitcnt vmcnt(2)
	v_mov_b64_e32 v[14:15], v[190:191]
	s_branch .LBB0_1228
